# v23
# speedup vs baseline: 1.0358x; 1.0060x over previous
.LBB0_5:
	v_mad_legacy_u16 v2, v6, s8, v4
	v_lshlrev_b16_e32 v8, 15, v2
	v_lshrrev_b16_e32 v2, 1, v2
	v_cmp_lt_u32_e32 vcc, s24, v6
	v_or_b32_e32 v2, v2, v8
	s_or_b64 s[0:1], vcc, s[0:1]
	v_cmp_gt_u16_e32 vcc, s9, v2
	v_add_u32_e32 v7, 0x200, v6
	v_mov_b32_e32 v6, v7
	v_cndmask_b32_e32 v2, 0, v5, vcc
	ds_write_b64 v1, v[2:3]
	v_add_u32_e32 v1, 0x1000, v1
	s_andn2_b64 exec, exec, s[0:1]
	s_cbranch_execnz .LBB0_5
	s_or_b64 exec, exec, s[0:1]
	s_mov_b32 s34, 0
	v_cmp_eq_u32_e64 s[0:1], 0, v0
	s_and_saveexec_b64 s[8:9], s[0:1]
	v_mov_b32_e32 v1, 8
	v_mov_b32_e32 v2, 0x23420
	ds_write_b32 v2, v1
	s_or_b64 exec, exec, s[8:9]
	v_lshlrev_b32_e32 v1, 2, v131
	v_or_b32_e32 v2, 0x22200, v1
	v_or_b32_e32 v3, 0x22300, v1
	s_waitcnt lgkmcnt(0)
	s_barrier
	ds_read_b32 v2, v2
	ds_read_b32 v3, v3
	v_and_b32_e32 v202, 15, v0
	s_lshl_b32 s30, s31, 4
	v_or_b32_e32 v132, s30, v202
	s_waitcnt lgkmcnt(0)
	v_add_f32_e32 v2, v2, v3
	v_mbcnt_lo_u32_b32 v3, -1, 0
	v_mbcnt_hi_u32_b32 v3, -1, v3
	v_and_b32_e32 v4, 64, v3
	v_add_u32_e32 v4, 64, v4
	v_xor_b32_e32 v5, 32, v3
	v_cmp_lt_i32_e32 vcc, v5, v4
	v_mov_b32_e32 v133, 0
	v_lshrrev_b32_e32 v209, 4, v131
	v_cndmask_b32_e32 v5, v3, v5, vcc
	v_lshlrev_b32_e32 v200, 2, v5
	v_mov_b32_e32 v100, v133
	v_mov_b32_e32 v101, v133
	v_and_b32_e32 v203, 48, v0
	v_mov_b32_e32 v98, v133
	v_xor_b32_e32 v5, 16, v3
	v_cmp_lt_i32_e32 vcc, v5, v4
	v_mov_b32_e32 v99, v133
	v_mov_b64_e32 v[104:105], v[100:101]
	v_cndmask_b32_e32 v5, v3, v5, vcc
	v_lshlrev_b32_e32 v201, 2, v5
	v_mov_b64_e32 v[108:109], v[100:101]
	v_mov_b64_e32 v[112:113], v[100:101]
	v_mov_b64_e32 v[116:117], v[100:101]
	v_mov_b64_e32 v[120:121], v[100:101]
	v_xor_b32_e32 v5, 8, v3
	v_cmp_lt_i32_e32 vcc, v5, v4
	v_mov_b64_e32 v[124:125], v[100:101]
	v_mov_b64_e32 v[128:129], v[100:101]
	v_cndmask_b32_e32 v5, v3, v5, vcc
	v_lshlrev_b32_e32 v205, 2, v5
	v_cmp_eq_u32_e64 s[8:9], 0, v131
	v_mov_b32_e32 v218, 0xff800000
	v_mov_b32_e32 v213, 0x23420
	v_mov_b64_e32 v[102:103], v[98:99]
	v_xor_b32_e32 v5, 4, v3
	v_cmp_lt_i32_e32 vcc, v5, v4
	v_mov_b64_e32 v[106:107], v[98:99]
	v_mov_b64_e32 v[110:111], v[98:99]
	v_cndmask_b32_e32 v5, v3, v5, vcc
	v_lshlrev_b32_e32 v206, 2, v5
	v_mov_b64_e32 v[114:115], v[98:99]
	v_mov_b64_e32 v[118:119], v[98:99]
	v_mov_b64_e32 v[122:123], v[98:99]
	v_mov_b64_e32 v[126:127], v[98:99]
	v_xor_b32_e32 v5, 2, v3
	v_cmp_lt_i32_e32 vcc, v5, v4
	v_mov_b32_e32 v219, 0
	s_mov_b32 s35, s31
	v_cndmask_b32_e32 v5, v3, v5, vcc
	v_lshlrev_b32_e32 v207, 2, v5
	v_mov_b32_e32 v138, 0
	v_mov_b32_e32 v139, v133
	v_mov_b32_e32 v136, 0
	v_mov_b32_e32 v137, v133
	v_xor_b32_e32 v5, 1, v3
	v_cmp_lt_i32_e32 vcc, v5, v4
	v_lshlrev_b32_e32 v4, 3, v131
	v_mov_b32_e32 v144, 0
	v_cndmask_b32_e32 v3, v3, v5, vcc
	v_lshlrev_b32_e32 v208, 2, v3
	v_mov_b32_e32 v145, v133
	v_mov_b32_e32 v142, 0
	v_mov_b32_e32 v143, v133
	v_mov_b32_e32 v150, 0
	s_nop 1
	v_add_f32_dpp v2, v2, v2 row_shr:1 row_mask:0xf bank_mask:0xf
	s_nop 1
	v_add_f32_dpp v2, v2, v2 row_shr:2 row_mask:0xf bank_mask:0xf
	s_nop 1
	v_add_f32_dpp v2, v2, v2 row_shr:4 row_mask:0xf bank_mask:0xf
	s_nop 1
	v_add_f32_dpp v2, v2, v2 row_shr:8 row_mask:0xf bank_mask:0xf
	s_nop 1
	v_add_f32_dpp v2, v2, v2 row_bcast:15 row_mask:0xa bank_mask:0xf
	s_nop 1
	v_add_f32_dpp v2, v2, v2 row_bcast:31 row_mask:0xc bank_mask:0xf
	s_nop 1
	v_readlane_b32 s44, v2, 63
	s_nop 1
	v_mov_b32_e32 v2, s44
	v_add_f32_e32 v2, s43, v2
	s_mul_i32 s4, s31, 0x2200
	s_add_i32 s24, s4, 0x11000
	v_mul_f32_e32 v210, 0x3fb8aa3b, v2
	s_movk_i32 s4, 0x220
	v_mov_b32_e32 v2, s24
	v_mad_u32_u24 v5, v202, s4, v2
	v_lshlrev_b64 v[2:3], 9, v[132:133]
	v_lshl_add_u64 v[2:3], s[6:7], 0, v[2:3]
	v_lshlrev_b32_e32 v132, 5, v209
	v_add_u32_e32 v212, s24, v4
	v_mad_u32_u24 v211, v202, s4, v203
	v_lshl_add_u64 v[134:135], v[2:3], 0, v[132:133]
	v_cmp_eq_u32_e64 s[6:7], 15, v202
	v_cmp_eq_u32_e64 s[4:5], 15, v131
	v_add_u32_e32 v214, v5, v203
	v_add_u32_e32 v215, 0x800, v212
	v_add_u32_e32 v216, 0x1000, v212
	v_add_u32_e32 v217, 0x1800, v212
	v_mov_b32_e32 v151, v133
	v_mov_b32_e32 v140, 0
	v_mov_b32_e32 v141, v133
	v_mov_b32_e32 v148, 0
	v_mov_b32_e32 v149, v133
	v_mov_b32_e32 v146, 0
	v_mov_b32_e32 v147, v133
	v_mov_b32_e32 v178, 0
	v_mov_b32_e32 v179, v133
	v_mov_b32_e32 v168, 0
	v_mov_b32_e32 v169, v133
	v_mov_b32_e32 v154, 0
	v_mov_b32_e32 v155, v133
	v_mov_b32_e32 v152, 0
	v_mov_b32_e32 v153, v133
	v_mov_b32_e32 v182, 0
	v_mov_b32_e32 v183, v133
	v_mov_b32_e32 v180, 0
	v_mov_b32_e32 v181, v133
	v_mov_b32_e32 v158, 0
	v_mov_b32_e32 v159, v133
	v_mov_b32_e32 v156, 0
	v_mov_b32_e32 v157, v133
	v_mov_b32_e32 v186, 0
	v_mov_b32_e32 v187, v133
	v_mov_b32_e32 v184, 0
	v_mov_b32_e32 v185, v133
	v_mov_b32_e32 v162, 0
	v_mov_b32_e32 v163, v133
	v_mov_b32_e32 v160, 0
	v_mov_b32_e32 v161, v133
	v_mov_b32_e32 v190, 0
	v_mov_b32_e32 v191, v133
	v_mov_b32_e32 v188, 0
	v_mov_b32_e32 v189, v133
	v_mov_b32_e32 v166, 0
	v_mov_b32_e32 v167, v133
	v_mov_b32_e32 v164, 0
	v_mov_b32_e32 v165, v133
	v_mov_b32_e32 v194, 0
	v_mov_b32_e32 v195, v133
	v_mov_b32_e32 v192, 0
	v_mov_b32_e32 v193, v133
	v_mov_b32_e32 v172, 0
	v_mov_b32_e32 v173, v133
	v_mov_b32_e32 v170, 0
	v_mov_b32_e32 v171, v133
	v_mov_b32_e32 v198, 0
	v_mov_b32_e32 v199, v133
	v_mov_b32_e32 v196, 0
	v_mov_b32_e32 v197, v133
	v_mov_b32_e32 v176, 0
	v_mov_b32_e32 v177, v133
	v_mov_b32_e32 v174, 0
	v_mov_b32_e32 v175, v133
	s_cmp_eq_u32 s2, 0
	s_cselect_b64 s[24:25], -1, 0
	s_and_b64 s[24:25], s[24:25], s[10:11]
	s_and_saveexec_b64 s[26:27], s[24:25]
	s_cbranch_execz .Lp1_noinit
	global_store_dword v[254:255], v253, off
